# layer-0 in-proj phase conversion slots re-tried now that a conversion item has all its loads in flight (WGs 0-127 one item per wave at phase start, WGs 128-255 a second item in the idle tail; prologue
# speedup vs baseline: 1.0012x; 1.0012x over previous
.LBB0_41:
	v_writelane_b32 v253, s24, 32
	v_writelane_b32 v253, s23, 34
	v_writelane_b32 v253, s22, 36
	s_mov_b32 s3, 0
	v_readlane_b32 s0, v253, 29
	s_lshl_b32 s0, s0, 14
	s_add_i32 s29, s0, 0
	s_cmp_lg_u64 s[48:49], 0
	v_readlane_b32 s4, v253, 30
	s_cselect_b64 s[44:45], -1, 0
	s_abs_i32 s2, s4
	v_cvt_f32_u32_e32 v2, s2
	s_sub_i32 s0, 0, s2
	s_ashr_i32 s6, s4, 31
	v_rcp_iflag_f32_e32 v2, v2
	s_nop 0
	v_mul_f32_e32 v2, 0x4f7ffffe, v2
	v_cvt_u32_f32_e32 v2, v2
	s_nop 0
	v_readfirstlane_b32 s1, v2
	s_mul_i32 s0, s0, s1
	s_mul_hi_u32 s0, s1, s0
	s_add_i32 s7, s1, s0
	s_mul_hi_u32 s0, s7, 0x4200
	s_mul_i32 s0, s0, s2
	s_sub_i32 s0, 0x4200, s0
	s_sub_i32 s1, s0, s2
	s_cmp_ge_u32 s0, s2
	s_cselect_b32 s0, s1, s0
	s_sub_i32 s1, s0, s2
	s_cmp_ge_u32 s0, s2
	s_cselect_b32 s8, s1, s0
	s_add_i32 s0, s4, 0xffffff00
	s_cmp_ge_i32 s0, s8
	s_cselect_b64 s[0:1], -1, 0
	s_cmpk_lt_u32 s8, 0x2101
	s_cselect_b64 s[4:5], -1, 0
	s_sub_i32 s8, 0x4200, s8
	s_and_b64 s[0:1], s[0:1], s[4:5]
	s_and_b64 s[0:1], s[0:1], exec
	s_cselect_b32 s5, s8, 0x4200
	s_add_i32 s0, s5, 0xffffda00
	s_cmp_eq_u32 s2, 0x800
	s_cselect_b32 s5, s0, s5
	v_writelane_b32 v253, s5, 38
	v_writelane_b32 v253, s48, 40
	s_mul_hi_u32 s0, s5, s7
	s_mul_i32 s1, s0, s2
	v_writelane_b32 v253, s49, 41
	v_writelane_b32 v253, s50, 42
	v_writelane_b32 v253, s51, 43
	v_writelane_b32 v253, s52, 44
	v_writelane_b32 v253, s53, 45
	v_writelane_b32 v253, s54, 46
	v_writelane_b32 v253, s55, 47
	s_sub_i32 s1, s5, s1
	v_writelane_b32 v253, s56, 48
	s_add_i32 s4, s0, 1
	s_sub_i32 s5, s1, s2
	v_writelane_b32 v253, s57, 49
	s_cmp_ge_u32 s1, s2
	v_writelane_b32 v253, s58, 50
	s_cselect_b32 s0, s4, s0
	v_writelane_b32 v253, s59, 51
	s_cselect_b32 s1, s5, s1
	s_add_i32 s4, s0, 1
	v_writelane_b32 v253, s60, 52
	s_cmp_ge_u32 s1, s2
	v_writelane_b32 v253, s61, 53
	s_cselect_b32 s0, s4, s0
	v_writelane_b32 v253, s62, 54
	s_xor_b32 s0, s0, s6
	v_writelane_b32 v253, s63, 55
	s_sub_i32 s15, s0, s6
	v_writelane_b32 v253, s29, 56
	s_add_i32 s14, s15, -2
	v_writelane_b32 v253, s44, 57
	s_cmp_lt_i32 s15, 1
	v_readfirstlane_b32 s0, v0
	v_writelane_b32 v253, s45, 58
	s_cbranch_scc1 .LBB0_65
	s_ashr_i32 s0, s0, 8
	s_min_i32 s18, s0, s14
	s_cmpk_gt_i32 s27, 0x7ff
	v_readlane_b32 s0, v253, 26
	s_cselect_b64 s[20:21], -1, 0
	s_add_u32 s0, s0, 0x800000
	v_writelane_b32 v253, s0, 59
	v_mov_b32_e32 v133, 0
	v_readlane_b32 s0, v253, 27
	s_addc_u32 s0, s0, 0
	s_add_i32 s25, 0, 0x21000
	v_writelane_b32 v253, s0, 61
	s_add_i32 s0, 0, 0x21200
	v_writelane_b32 v253, s0, 63
	s_add_i32 s0, 0, 0x21100
	v_writelane_b32 v254, s0, 1
	s_add_i32 s0, 0, 0x21300
	v_writelane_b32 v254, s0, 3
	v_writelane_b32 v254, s27, 5
	v_writelane_b32 v254, s14, 7
	v_writelane_b32 v254, s15, 9
	v_writelane_b32 v254, s18, 11
	v_writelane_b32 v254, s20, 13
	s_mov_b32 s22, 0x42800000
	s_mov_b32 s19, 0
	v_writelane_b32 v254, s21, 14
	s_branch .LBB0_45
